# odd XCDs start the merge-to-w_xo window one s_sleep late (de-phases HBM-bound residual epilogues across XCDs)
# speedup vs baseline: 1.0045x; 1.0045x over previous
; #define OPAQUE_WS() unsigned char* ws = P.ws; asm volatile("" : "+s"(ws)); F.ws = ws; F.tid = fresh_tid(F.wave); asm volatile("" : "+v"(F.tid)); F.lane = F.tid & 63; int c = F.bid; asm volatile("" : "+s"(c))
; #define REP_BEGIN(k) for (int rep_ = 0, nrep_ = ((k) >= PROBE_LO && (k) < PROBE_HI) ? PROBE_N : 0; rep_ <= nrep_; ++rep_) { const bool rerun = PROBE_AFTER ? (rep_ > 0) : (rep_ < nrep_), dry = rerun && PROBE_DRY_;
;     __device__ __forceinline__ bool next(int i, pg8::Unit& u) const {
;         const int t = i / 3, sub = i - 3 * t; const long L = (long)t * G + c; if (L >= (long)nM * nN) return false;
;         pg8::tile_order((int)L, nM, nN, u.pm, u.pn); u.sub = sub;
;         const size_t ao = sub == 0 ? AR_QA : sub == 1 ? AR_PB : AR_QC;
;         u.a = (const char*)ws + ao + (size_t)u.pm * 256 * K * 2; u.b = (const char*)ws + WB_WBR + (size_t)(l * 3 + sub) * SZ_WBR + (size_t)u.pn * 256 * K * 2; return true;
;     }
; __global__ void __launch_bounds__(NTHREADS, 2) mk_fwd(Params P) {
;     ...
;         if (PH_EN(2) && IN(pb + 2)) { REP_BEGIN(pb + 2) OPAQUE_WS(); int lq = l; asm volatile("" : "+s"(lq));
;             SchedMerge Sg{ws, lq, NTOK / 256, D / 256, 512, G, c};
;             EpiMerge E{ws, dry};
;             pg8::gemm_phase<EpiMerge, SchedMerge>(F.lds, 512, Sg, E, F.wave);
.LBB0_947:
	s_or_b64 exec, exec, s[0:1]
	v_readlane_b32 s0, v253, 0
	s_bitcmp1_b32 s100, 0
	s_cbranch_scc0 .Lxs_done
	s_bitcmp1_b32 s0, 0
	s_cbranch_scc0 .Lxs_done
	s_movk_i32 s0, 1
